# final-output (d_out) stores of the last MoE phase write-through sc1 instead of non-temporal
# baseline (speedup 1.0000x reference)
.LBB0_2178:
	v_cmp_gt_i32_e64 s[14:15], s58, v185
	v_cmp_gt_i32_e64 s[12:13], s58, v186
	v_cmp_gt_i32_e64 s[10:11], s58, v187
	v_cndmask_b32_e64 v128, 0, v185, s[14:15]
	v_add_u32_e32 v128, s80, v128
	v_cndmask_b32_e64 v130, 0, v186, s[12:13]
	v_cndmask_b32_e64 v132, 0, v187, s[10:11]
	v_ashrrev_i32_e32 v129, 31, v128
	v_add_u32_e32 v130, s80, v130
	v_add_u32_e32 v132, s80, v132
	v_lshl_add_u64 v[128:129], v[128:129], 2, s[24:25]
	v_ashrrev_i32_e32 v131, 31, v130
	v_ashrrev_i32_e32 v133, 31, v132
	v_lshl_add_u64 v[130:131], v[130:131], 2, s[24:25]
	v_lshl_add_u64 v[132:133], v[132:133], 2, s[24:25]
	global_load_dword v178, v[128:129], off
	global_load_dword v176, v[130:131], off
	global_load_dword v174, v[132:133], off
	v_cmp_gt_i32_e64 s[8:9], s58, v188
	v_cmp_gt_i32_e64 s[6:7], s58, v189
	v_cmp_gt_i32_e64 s[4:5], s58, v190
	v_cndmask_b32_e64 v128, 0, v188, s[8:9]
	v_cndmask_b32_e64 v129, 0, v189, s[6:7]
	v_cmp_gt_i32_e32 vcc, s58, v191
	v_cndmask_b32_e64 v131, 0, v190, s[4:5]
	v_add_u32_e32 v128, s80, v128
	v_cndmask_b32_e32 v133, 0, v191, vcc
	v_add_u32_e32 v130, s80, v129
	v_lshl_or_b32 v162, s16, 8, v192
	v_add_u32_e32 v132, s80, v131
	v_add_u32_e32 v134, s80, v133
	v_ashrrev_i32_e32 v129, 31, v128
	v_ashrrev_i32_e32 v131, 31, v130
	v_ashrrev_i32_e32 v163, 31, v162
	v_ashrrev_i32_e32 v133, 31, v132
	v_ashrrev_i32_e32 v135, 31, v134
	v_lshl_add_u64 v[128:129], v[128:129], 2, s[24:25]
	v_lshl_add_u64 v[130:131], v[130:131], 2, s[24:25]
	v_lshl_add_u64 v[172:173], v[162:163], 1, s[82:83]
	v_lshl_add_u64 v[132:133], v[132:133], 2, s[24:25]
	v_lshl_add_u64 v[134:135], v[134:135], 2, s[24:25]
	global_load_dword v170, v[128:129], off
	global_load_dword v168, v[130:131], off
	global_load_dword v166, v[132:133], off
	global_load_dword v164, v[134:135], off
	v_cmp_gt_i32_e64 s[16:17], s58, v180
	s_waitcnt vmcnt(0)
	v_ashrrev_i32_e32 v179, 31, v178
	v_ashrrev_i32_e32 v177, 31, v176
	v_ashrrev_i32_e32 v175, 31, v174
	v_lshlrev_b64 v[128:129], 11, v[178:179]
	v_lshlrev_b64 v[130:131], 11, v[176:177]
	v_lshlrev_b64 v[132:133], 11, v[174:175]
	v_lshl_add_u64 v[128:129], v[172:173], 0, v[128:129]
	v_lshl_add_u64 v[130:131], v[172:173], 0, v[130:131]
	v_lshl_add_u64 v[196:197], v[172:173], 0, v[132:133]
	global_load_dwordx4 v[148:151], v[128:129], off
	global_load_dwordx4 v[144:147], v[128:129], off offset:256
	global_load_dwordx4 v[140:143], v[130:131], off
	global_load_dwordx4 v[136:139], v[130:131], off offset:256
	global_load_dwordx4 v[132:135], v[196:197], off
	s_nop 0
	global_load_dwordx4 v[128:131], v[196:197], off offset:256
	s_and_saveexec_b64 s[58:59], s[16:17]
	s_cbranch_execz .LBB0_2182
	v_add_u32_e32 v196, s80, v180
	v_ashrrev_i32_e32 v197, 31, v196
	v_lshl_add_u64 v[196:197], v[196:197], 2, s[24:25]
	global_load_dword v204, v[196:197], off
	v_readlane_b32 s36, v253, 46
	v_readlane_b32 s48, v253, 58
	v_readlane_b32 s49, v253, 59
	v_readlane_b32 s37, v253, 47
	v_readlane_b32 s38, v253, 48
	v_readlane_b32 s39, v253, 49
	v_readlane_b32 s40, v253, 50
	v_readlane_b32 s41, v253, 51
	v_readlane_b32 s42, v253, 52
	v_readlane_b32 s43, v253, 53
	v_readlane_b32 s44, v253, 54
	v_readlane_b32 s45, v253, 55
	v_readlane_b32 s46, v253, 56
	v_readlane_b32 s47, v253, 57
	v_readlane_b32 s50, v253, 60
	v_readlane_b32 s51, v253, 61
	s_waitcnt vmcnt(0)
	v_ashrrev_i32_e32 v205, 31, v204
	v_lshlrev_b64 v[196:197], 11, v[204:205]
	v_lshl_add_u64 v[200:201], v[172:173], 0, v[196:197]
	global_load_dwordx4 v[196:199], v[200:201], off
	s_nop 0
	global_load_dwordx4 v[200:203], v[200:201], off offset:256
	v_lshlrev_b64 v[204:205], 12, v[204:205]
	v_lshl_add_u64 v[204:205], s[48:49], 0, v[204:205]
	v_lshl_add_u64 v[204:205], v[162:163], 2, v[204:205]
	s_waitcnt vmcnt(0)
	v_lshlrev_b32_e32 v206, 16, v196
	v_and_b32_e32 v207, 0xffff0000, v196
	v_lshlrev_b32_e32 v196, 16, v197
	v_and_b32_e32 v197, 0xffff0000, v197
	v_lshlrev_b32_e32 v208, 16, v198
	v_and_b32_e32 v209, 0xffff0000, v198
	v_lshlrev_b32_e32 v198, 16, v199
	v_and_b32_e32 v199, 0xffff0000, v199
	v_lshlrev_b32_e32 v210, 16, v200
	v_and_b32_e32 v211, 0xffff0000, v200
	v_lshlrev_b32_e32 v200, 16, v201
	v_and_b32_e32 v201, 0xffff0000, v201
	v_lshlrev_b32_e32 v212, 16, v202
	v_and_b32_e32 v213, 0xffff0000, v202
	v_lshlrev_b32_e32 v202, 16, v203
	v_and_b32_e32 v203, 0xffff0000, v203
	v_pk_add_f32 v[126:127], v[126:127], v[196:197]
	v_pk_add_f32 v[124:125], v[124:125], v[206:207]
	v_pk_add_f32 v[122:123], v[122:123], v[198:199]
	v_pk_add_f32 v[120:121], v[120:121], v[208:209]
	v_pk_add_f32 v[118:119], v[118:119], v[200:201]
	v_pk_add_f32 v[116:117], v[116:117], v[210:211]
	v_pk_add_f32 v[114:115], v[114:115], v[202:203]
	v_pk_add_f32 v[112:113], v[112:113], v[212:213]
	global_store_dwordx4 v[204:205], v[124:127], off sc1
	global_store_dwordx4 v[204:205], v[120:123], off offset:16 sc1
	global_store_dwordx4 v[204:205], v[116:119], off offset:512 sc1
	global_store_dwordx4 v[204:205], v[112:115], off offset:528 sc1
	s_or_b64 exec, exec, s[58:59]
	s_and_saveexec_b64 s[16:17], s[14:15]
	s_cbranch_execnz .LBB0_2183

.LBB0_2181:
	v_lshlrev_b32_e32 v96, 16, v140
	v_and_b32_e32 v97, 0xffff0000, v140
	v_pk_add_f32 v[92:93], v[92:93], v[96:97]
	v_lshlrev_b32_e32 v96, 16, v142
	v_and_b32_e32 v97, 0xffff0000, v142
	v_readlane_b32 s36, v253, 46
	v_lshlrev_b32_e32 v98, 16, v141
	v_and_b32_e32 v99, 0xffff0000, v141
	v_pk_add_f32 v[88:89], v[88:89], v[96:97]
	v_lshlrev_b64 v[96:97], 12, v[176:177]
	v_readlane_b32 s48, v253, 58
	v_readlane_b32 s49, v253, 59
	v_pk_add_f32 v[94:95], v[94:95], v[98:99]
	v_lshlrev_b32_e32 v98, 16, v143
	v_and_b32_e32 v99, 0xffff0000, v143
	v_lshl_add_u64 v[96:97], s[48:49], 0, v[96:97]
	v_pk_add_f32 v[90:91], v[90:91], v[98:99]
	v_lshl_add_u64 v[96:97], v[162:163], 2, v[96:97]
	global_store_dwordx4 v[96:97], v[92:95], off sc1
	global_store_dwordx4 v[96:97], v[88:91], off offset:16 sc1
	v_readlane_b32 s37, v253, 47
	v_readlane_b32 s38, v253, 48
	v_lshlrev_b32_e32 v88, 16, v136
	v_and_b32_e32 v89, 0xffff0000, v136
	v_lshlrev_b32_e32 v90, 16, v137
	v_and_b32_e32 v91, 0xffff0000, v137
	v_pk_add_f32 v[86:87], v[86:87], v[90:91]
	v_pk_add_f32 v[84:85], v[84:85], v[88:89]
	v_lshlrev_b32_e32 v88, 16, v138
	v_and_b32_e32 v89, 0xffff0000, v138
	v_lshlrev_b32_e32 v90, 16, v139
	v_and_b32_e32 v91, 0xffff0000, v139
	v_readlane_b32 s39, v253, 49
	v_readlane_b32 s40, v253, 50
	v_readlane_b32 s41, v253, 51
	v_readlane_b32 s42, v253, 52
	v_readlane_b32 s43, v253, 53
	v_readlane_b32 s44, v253, 54
	v_readlane_b32 s45, v253, 55
	v_readlane_b32 s46, v253, 56
	v_readlane_b32 s47, v253, 57
	v_readlane_b32 s50, v253, 60
	v_readlane_b32 s51, v253, 61
	v_pk_add_f32 v[82:83], v[82:83], v[90:91]
	v_pk_add_f32 v[80:81], v[80:81], v[88:89]
	global_store_dwordx4 v[96:97], v[84:87], off offset:512 sc1
	global_store_dwordx4 v[96:97], v[80:83], off offset:528 sc1
	s_or_b64 exec, exec, s[14:15]
	s_and_saveexec_b64 s[12:13], s[10:11]
	s_cbranch_execnz .LBB0_2185
	s_branch .LBB0_2186

.LBB0_2183:
	v_lshlrev_b32_e32 v112, 16, v148
	v_and_b32_e32 v113, 0xffff0000, v148
	v_pk_add_f32 v[108:109], v[108:109], v[112:113]
	v_lshlrev_b32_e32 v112, 16, v150
	v_and_b32_e32 v113, 0xffff0000, v150
	v_readlane_b32 s36, v253, 46
	v_lshlrev_b32_e32 v114, 16, v149
	v_and_b32_e32 v115, 0xffff0000, v149
	v_pk_add_f32 v[104:105], v[104:105], v[112:113]
	v_lshlrev_b64 v[112:113], 12, v[178:179]
	v_readlane_b32 s48, v253, 58
	v_readlane_b32 s49, v253, 59
	v_pk_add_f32 v[110:111], v[110:111], v[114:115]
	v_lshlrev_b32_e32 v114, 16, v151
	v_and_b32_e32 v115, 0xffff0000, v151
	v_lshl_add_u64 v[112:113], s[48:49], 0, v[112:113]
	v_pk_add_f32 v[106:107], v[106:107], v[114:115]
	v_lshl_add_u64 v[112:113], v[162:163], 2, v[112:113]
	global_store_dwordx4 v[112:113], v[108:111], off sc1
	global_store_dwordx4 v[112:113], v[104:107], off offset:16 sc1
	v_readlane_b32 s37, v253, 47
	v_readlane_b32 s38, v253, 48
	v_lshlrev_b32_e32 v104, 16, v144
	v_and_b32_e32 v105, 0xffff0000, v144
	v_lshlrev_b32_e32 v106, 16, v145
	v_and_b32_e32 v107, 0xffff0000, v145
	v_pk_add_f32 v[102:103], v[102:103], v[106:107]
	v_pk_add_f32 v[100:101], v[100:101], v[104:105]
	v_lshlrev_b32_e32 v104, 16, v146
	v_and_b32_e32 v105, 0xffff0000, v146
	v_lshlrev_b32_e32 v106, 16, v147
	v_and_b32_e32 v107, 0xffff0000, v147
	v_readlane_b32 s39, v253, 49
	v_readlane_b32 s40, v253, 50
	v_readlane_b32 s41, v253, 51
	v_readlane_b32 s42, v253, 52
	v_readlane_b32 s43, v253, 53
	v_readlane_b32 s44, v253, 54
	v_readlane_b32 s45, v253, 55
	v_readlane_b32 s46, v253, 56
	v_readlane_b32 s47, v253, 57
	v_readlane_b32 s50, v253, 60
	v_readlane_b32 s51, v253, 61
	v_pk_add_f32 v[98:99], v[98:99], v[106:107]
	v_pk_add_f32 v[96:97], v[96:97], v[104:105]
	global_store_dwordx4 v[112:113], v[100:103], off offset:512 sc1
	global_store_dwordx4 v[112:113], v[96:99], off offset:528 sc1
	s_or_b64 exec, exec, s[16:17]
	s_and_saveexec_b64 s[14:15], s[12:13]
	s_cbranch_execnz .LBB0_2181

.LBB0_2185:
	v_lshlrev_b32_e32 v80, 16, v132
	v_and_b32_e32 v81, 0xffff0000, v132
	v_pk_add_f32 v[76:77], v[76:77], v[80:81]
	v_lshlrev_b32_e32 v80, 16, v134
	v_and_b32_e32 v81, 0xffff0000, v134
	v_readlane_b32 s36, v253, 46
	v_lshlrev_b32_e32 v82, 16, v133
	v_and_b32_e32 v83, 0xffff0000, v133
	v_pk_add_f32 v[72:73], v[72:73], v[80:81]
	v_lshlrev_b64 v[80:81], 12, v[174:175]
	v_readlane_b32 s48, v253, 58
	v_readlane_b32 s49, v253, 59
	v_pk_add_f32 v[78:79], v[78:79], v[82:83]
	v_lshlrev_b32_e32 v82, 16, v135
	v_and_b32_e32 v83, 0xffff0000, v135
	v_lshl_add_u64 v[80:81], s[48:49], 0, v[80:81]
	v_pk_add_f32 v[74:75], v[74:75], v[82:83]
	v_lshl_add_u64 v[80:81], v[162:163], 2, v[80:81]
	global_store_dwordx4 v[80:81], v[76:79], off sc1
	global_store_dwordx4 v[80:81], v[72:75], off offset:16 sc1
	v_readlane_b32 s37, v253, 47
	v_readlane_b32 s38, v253, 48
	v_lshlrev_b32_e32 v72, 16, v128
	v_and_b32_e32 v73, 0xffff0000, v128
	v_lshlrev_b32_e32 v74, 16, v129
	v_and_b32_e32 v75, 0xffff0000, v129
	v_pk_add_f32 v[70:71], v[70:71], v[74:75]
	v_pk_add_f32 v[68:69], v[68:69], v[72:73]
	v_lshlrev_b32_e32 v72, 16, v130
	v_and_b32_e32 v73, 0xffff0000, v130
	v_lshlrev_b32_e32 v74, 16, v131
	v_and_b32_e32 v75, 0xffff0000, v131
	v_readlane_b32 s39, v253, 49
	v_readlane_b32 s40, v253, 50
	v_readlane_b32 s41, v253, 51
	v_readlane_b32 s42, v253, 52
	v_readlane_b32 s43, v253, 53
	v_readlane_b32 s44, v253, 54
	v_readlane_b32 s45, v253, 55
	v_readlane_b32 s46, v253, 56
	v_readlane_b32 s47, v253, 57
	v_readlane_b32 s50, v253, 60
	v_readlane_b32 s51, v253, 61
	v_pk_add_f32 v[66:67], v[66:67], v[74:75]
	v_pk_add_f32 v[64:65], v[64:65], v[72:73]
	global_store_dwordx4 v[80:81], v[68:71], off offset:512 sc1
	global_store_dwordx4 v[80:81], v[64:67], off offset:528 sc1
.LBB0_2186:
	s_or_b64 exec, exec, s[12:13]
	v_ashrrev_i32_e32 v169, 31, v168
	v_lshlrev_b64 v[64:65], 11, v[168:169]
	v_lshl_add_u64 v[64:65], v[172:173], 0, v[64:65]
	v_ashrrev_i32_e32 v167, 31, v166
	global_load_dwordx4 v[84:87], v[64:65], off
	global_load_dwordx4 v[80:83], v[64:65], off offset:256
	v_lshlrev_b64 v[64:65], 11, v[166:167]
	v_lshl_add_u64 v[64:65], v[172:173], 0, v[64:65]
	v_ashrrev_i32_e32 v165, 31, v164
	global_load_dwordx4 v[76:79], v[64:65], off
	global_load_dwordx4 v[72:75], v[64:65], off offset:256
	v_lshlrev_b64 v[64:65], 11, v[164:165]
	v_lshl_add_u64 v[64:65], v[172:173], 0, v[64:65]
	global_load_dwordx4 v[68:71], v[64:65], off
	s_nop 0
	global_load_dwordx4 v[64:67], v[64:65], off offset:256
	s_and_saveexec_b64 s[10:11], s[8:9]
	s_cbranch_execz .LBB0_2191
	v_ashrrev_i32_e32 v171, 31, v170
	v_lshlrev_b64 v[88:89], 11, v[170:171]
	v_lshl_add_u64 v[92:93], v[172:173], 0, v[88:89]
	global_load_dwordx4 v[88:91], v[92:93], off
	s_nop 0
	global_load_dwordx4 v[92:95], v[92:93], off offset:256
	v_readlane_b32 s36, v253, 46
	v_lshlrev_b64 v[96:97], 12, v[170:171]
	v_readlane_b32 s48, v253, 58
	v_readlane_b32 s49, v253, 59
	v_readlane_b32 s37, v253, 47
	v_readlane_b32 s38, v253, 48
	v_lshl_add_u64 v[96:97], s[48:49], 0, v[96:97]
	v_lshl_add_u64 v[96:97], v[162:163], 2, v[96:97]
	v_readlane_b32 s39, v253, 49
	v_readlane_b32 s40, v253, 50
	v_readlane_b32 s41, v253, 51
	v_readlane_b32 s42, v253, 52
	v_readlane_b32 s43, v253, 53
	v_readlane_b32 s44, v253, 54
	v_readlane_b32 s45, v253, 55
	v_readlane_b32 s46, v253, 56
	v_readlane_b32 s47, v253, 57
	v_readlane_b32 s50, v253, 60
	v_readlane_b32 s51, v253, 61
	s_waitcnt vmcnt(0)
	v_lshlrev_b32_e32 v98, 16, v88
	v_and_b32_e32 v99, 0xffff0000, v88
	v_lshlrev_b32_e32 v88, 16, v89
	v_and_b32_e32 v89, 0xffff0000, v89
	v_lshlrev_b32_e32 v100, 16, v90
	v_and_b32_e32 v101, 0xffff0000, v90
	v_lshlrev_b32_e32 v90, 16, v91
	v_and_b32_e32 v91, 0xffff0000, v91
	v_lshlrev_b32_e32 v102, 16, v92
	v_and_b32_e32 v103, 0xffff0000, v92
	v_lshlrev_b32_e32 v92, 16, v93
	v_and_b32_e32 v93, 0xffff0000, v93
	v_lshlrev_b32_e32 v104, 16, v94
	v_and_b32_e32 v105, 0xffff0000, v94
	v_lshlrev_b32_e32 v94, 16, v95
	v_and_b32_e32 v95, 0xffff0000, v95
	v_pk_add_f32 v[58:59], v[58:59], v[88:89]
	v_pk_add_f32 v[56:57], v[56:57], v[98:99]
	v_pk_add_f32 v[62:63], v[62:63], v[90:91]
	v_pk_add_f32 v[60:61], v[60:61], v[100:101]
	v_pk_add_f32 v[54:55], v[54:55], v[92:93]
	v_pk_add_f32 v[52:53], v[52:53], v[102:103]
	v_pk_add_f32 v[50:51], v[50:51], v[94:95]
	v_pk_add_f32 v[48:49], v[48:49], v[104:105]
	global_store_dwordx4 v[96:97], v[56:59], off sc1
	global_store_dwordx4 v[96:97], v[60:63], off offset:16 sc1
	global_store_dwordx4 v[96:97], v[52:55], off offset:512 sc1
	global_store_dwordx4 v[96:97], v[48:51], off offset:528 sc1
	s_or_b64 exec, exec, s[10:11]
	s_and_saveexec_b64 s[8:9], s[6:7]
	s_cbranch_execnz .LBB0_2192

.LBB0_2189:
	v_lshlrev_b32_e32 v32, 16, v76
	v_and_b32_e32 v33, 0xffff0000, v76
	v_pk_add_f32 v[28:29], v[28:29], v[32:33]
	v_lshlrev_b32_e32 v32, 16, v78
	v_and_b32_e32 v33, 0xffff0000, v78
	v_readlane_b32 s36, v253, 46
	v_lshlrev_b32_e32 v34, 16, v77
	v_and_b32_e32 v35, 0xffff0000, v77
	v_pk_add_f32 v[24:25], v[24:25], v[32:33]
	v_lshlrev_b64 v[32:33], 12, v[166:167]
	v_readlane_b32 s48, v253, 58
	v_readlane_b32 s49, v253, 59
	v_pk_add_f32 v[30:31], v[30:31], v[34:35]
	v_lshlrev_b32_e32 v34, 16, v79
	v_and_b32_e32 v35, 0xffff0000, v79
	v_lshl_add_u64 v[32:33], s[48:49], 0, v[32:33]
	v_pk_add_f32 v[26:27], v[26:27], v[34:35]
	v_lshl_add_u64 v[32:33], v[162:163], 2, v[32:33]
	global_store_dwordx4 v[32:33], v[28:31], off sc1
	global_store_dwordx4 v[32:33], v[24:27], off offset:16 sc1
	v_readlane_b32 s37, v253, 47
	v_readlane_b32 s38, v253, 48
	v_lshlrev_b32_e32 v24, 16, v72
	v_and_b32_e32 v25, 0xffff0000, v72
	v_lshlrev_b32_e32 v26, 16, v73
	v_and_b32_e32 v27, 0xffff0000, v73
	v_pk_add_f32 v[22:23], v[22:23], v[26:27]
	v_pk_add_f32 v[20:21], v[20:21], v[24:25]
	v_lshlrev_b32_e32 v24, 16, v74
	v_and_b32_e32 v25, 0xffff0000, v74
	v_lshlrev_b32_e32 v26, 16, v75
	v_and_b32_e32 v27, 0xffff0000, v75
	v_readlane_b32 s39, v253, 49
	v_readlane_b32 s40, v253, 50
	v_readlane_b32 s41, v253, 51
	v_readlane_b32 s42, v253, 52
	v_readlane_b32 s43, v253, 53
	v_readlane_b32 s44, v253, 54
	v_readlane_b32 s45, v253, 55
	v_readlane_b32 s46, v253, 56
	v_readlane_b32 s47, v253, 57
	v_readlane_b32 s50, v253, 60
	v_readlane_b32 s51, v253, 61
	v_pk_add_f32 v[18:19], v[18:19], v[26:27]
	v_pk_add_f32 v[16:17], v[16:17], v[24:25]
	global_store_dwordx4 v[32:33], v[20:23], off offset:512 sc1
	global_store_dwordx4 v[32:33], v[16:19], off offset:528 sc1
	s_or_b64 exec, exec, s[6:7]
	s_and_saveexec_b64 s[4:5], vcc
	s_cbranch_execnz .LBB0_2194

.LBB0_2192:
	v_lshlrev_b32_e32 v48, 16, v84
	v_and_b32_e32 v49, 0xffff0000, v84
	v_pk_add_f32 v[44:45], v[44:45], v[48:49]
	v_lshlrev_b32_e32 v48, 16, v86
	v_and_b32_e32 v49, 0xffff0000, v86
	v_readlane_b32 s36, v253, 46
	v_lshlrev_b32_e32 v50, 16, v85
	v_and_b32_e32 v51, 0xffff0000, v85
	v_pk_add_f32 v[40:41], v[40:41], v[48:49]
	v_lshlrev_b64 v[48:49], 12, v[168:169]
	v_readlane_b32 s48, v253, 58
	v_readlane_b32 s49, v253, 59
	v_pk_add_f32 v[46:47], v[46:47], v[50:51]
	v_lshlrev_b32_e32 v50, 16, v87
	v_and_b32_e32 v51, 0xffff0000, v87
	v_lshl_add_u64 v[48:49], s[48:49], 0, v[48:49]
	v_pk_add_f32 v[42:43], v[42:43], v[50:51]
	v_lshl_add_u64 v[48:49], v[162:163], 2, v[48:49]
	global_store_dwordx4 v[48:49], v[44:47], off sc1
	global_store_dwordx4 v[48:49], v[40:43], off offset:16 sc1
	v_readlane_b32 s37, v253, 47
	v_readlane_b32 s38, v253, 48
	v_lshlrev_b32_e32 v40, 16, v80
	v_and_b32_e32 v41, 0xffff0000, v80
	v_lshlrev_b32_e32 v42, 16, v81
	v_and_b32_e32 v43, 0xffff0000, v81
	v_pk_add_f32 v[38:39], v[38:39], v[42:43]
	v_pk_add_f32 v[36:37], v[36:37], v[40:41]
	v_lshlrev_b32_e32 v40, 16, v82
	v_and_b32_e32 v41, 0xffff0000, v82
	v_lshlrev_b32_e32 v42, 16, v83
	v_and_b32_e32 v43, 0xffff0000, v83
	v_readlane_b32 s39, v253, 49
	v_readlane_b32 s40, v253, 50
	v_readlane_b32 s41, v253, 51
	v_readlane_b32 s42, v253, 52
	v_readlane_b32 s43, v253, 53
	v_readlane_b32 s44, v253, 54
	v_readlane_b32 s45, v253, 55
	v_readlane_b32 s46, v253, 56
	v_readlane_b32 s47, v253, 57
	v_readlane_b32 s50, v253, 60
	v_readlane_b32 s51, v253, 61
	v_pk_add_f32 v[34:35], v[34:35], v[42:43]
	v_pk_add_f32 v[32:33], v[32:33], v[40:41]
	global_store_dwordx4 v[48:49], v[36:39], off offset:512 sc1
	global_store_dwordx4 v[48:49], v[32:35], off offset:528 sc1
	s_or_b64 exec, exec, s[8:9]
	s_and_saveexec_b64 s[6:7], s[4:5]
	s_cbranch_execnz .LBB0_2189

.LBB0_2194:
	v_lshlrev_b32_e32 v16, 16, v68
	v_and_b32_e32 v17, 0xffff0000, v68
	v_pk_add_f32 v[12:13], v[12:13], v[16:17]
	v_lshlrev_b32_e32 v16, 16, v70
	v_and_b32_e32 v17, 0xffff0000, v70
	v_readlane_b32 s36, v253, 46
	v_lshlrev_b32_e32 v18, 16, v69
	v_and_b32_e32 v19, 0xffff0000, v69
	v_pk_add_f32 v[8:9], v[8:9], v[16:17]
	v_lshlrev_b64 v[16:17], 12, v[164:165]
	v_readlane_b32 s48, v253, 58
	v_readlane_b32 s49, v253, 59
	v_pk_add_f32 v[14:15], v[14:15], v[18:19]
	v_lshlrev_b32_e32 v18, 16, v71
	v_and_b32_e32 v19, 0xffff0000, v71
	v_lshl_add_u64 v[16:17], s[48:49], 0, v[16:17]
	v_pk_add_f32 v[10:11], v[10:11], v[18:19]
	v_lshl_add_u64 v[16:17], v[162:163], 2, v[16:17]
	global_store_dwordx4 v[16:17], v[12:15], off sc1
	global_store_dwordx4 v[16:17], v[8:11], off offset:16 sc1
	v_readlane_b32 s37, v253, 47
	v_readlane_b32 s38, v253, 48
	v_lshlrev_b32_e32 v8, 16, v64
	v_and_b32_e32 v9, 0xffff0000, v64
	v_lshlrev_b32_e32 v10, 16, v65
	v_and_b32_e32 v11, 0xffff0000, v65
	v_pk_add_f32 v[6:7], v[6:7], v[10:11]
	v_pk_add_f32 v[4:5], v[4:5], v[8:9]
	v_lshlrev_b32_e32 v8, 16, v66
	v_and_b32_e32 v9, 0xffff0000, v66
	v_lshlrev_b32_e32 v10, 16, v67
	v_and_b32_e32 v11, 0xffff0000, v67
	v_readlane_b32 s39, v253, 49
	v_readlane_b32 s40, v253, 50
	v_readlane_b32 s41, v253, 51
	v_readlane_b32 s42, v253, 52
	v_readlane_b32 s43, v253, 53
	v_readlane_b32 s44, v253, 54
	v_readlane_b32 s45, v253, 55
	v_readlane_b32 s46, v253, 56
	v_readlane_b32 s47, v253, 57
	v_readlane_b32 s50, v253, 60
	v_readlane_b32 s51, v253, 61
	v_pk_add_f32 v[2:3], v[2:3], v[10:11]
	v_pk_add_f32 v[0:1], v[0:1], v[8:9]
	global_store_dwordx4 v[16:17], v[4:7], off offset:512 sc1
	global_store_dwordx4 v[16:17], v[0:3], off offset:528 sc1
	s_or_b64 exec, exec, s[4:5]
	s_and_b64 vcc, exec, s[2:3]
	s_mov_b64 s[2:3], -1
	s_cbranch_vccnz .LBB0_2121
